# speedup vs baseline: 1.0243x; 1.0243x over previous
.LBB0_181:
	s_load_dwordx4 s[4:7], s[0:1], 0x28
	s_add_i32 s3, s2, 0xffffe5a0
	s_and_b32 s10, s3, 0xff
	s_bitcmp0_b32 s3, 8
	v_mov_b32_e32 v3, 0
	s_waitcnt lgkmcnt(0)
	s_cselect_b32 s5, s5, s7
	s_cselect_b32 s4, s4, s6
	s_lshr_b32 s6, s3, 1
	s_and_b32 s6, s6, 0x100
	s_or_b32 s6, s6, s10
	s_mulk_i32 s6, 0x2400
	s_add_u32 s4, s4, s6
	s_addc_u32 s5, s5, 0
	v_lshlrev_b32_e32 v2, 2, v0
	v_lshl_add_u64 v[4:5], s[4:5], 0, v[2:3]
	global_load_dword v1, v2, s[4:5] nt
	global_load_dword v6, v2, s[4:5] offset:1024 nt
	global_load_dword v7, v2, s[4:5] offset:2048 nt
	global_load_dword v8, v2, s[4:5] offset:3072 nt
	v_or_b32_e32 v2, 0x400, v0
	s_movk_i32 s6, 0x1000
	v_lshlrev_b32_e32 v9, 2, v2
	v_add_co_u32_e32 v4, vcc, s6, v4
	v_or_b32_e32 v14, 0x100, v0
	s_nop 0
	v_addc_co_u32_e32 v5, vcc, 0, v5, vcc
	global_load_dword v10, v9, s[4:5] nt
	global_load_dword v11, v[4:5], off offset:1024 nt
	global_load_dword v12, v[4:5], off offset:2048 nt
	global_load_dword v13, v[4:5], off offset:3072 nt
	v_or_b32_e32 v4, 0x800, v0
	v_lshlrev_b32_e32 v5, 2, v4
	global_load_dword v5, v5, s[4:5] nt
	s_movk_i32 s11, 0x480
	v_mul_u32_u24_e32 v14, 0x1c72, v0
	v_lshrrev_b32_e32 v14, 16, v14
	v_mul_u32_u24_e32 v15, 9, v14
	v_sub_u32_e32 v15, v0, v15
	v_lshrrev_b32_e32 v16, 6, v14
	v_and_b32_e32 v14, 63, v14
	v_lshlrev_b32_e32 v15, 7, v15
	v_lshl_or_b32 v15, v14, 1, v15
	v_mad_u32_u24 v20, v16, s11, v15
	v_or_b32_e32 v17, 0x100, v0
	v_mul_u32_u24_e32 v14, 0x1c72, v17
	v_lshrrev_b32_e32 v14, 16, v14
	v_mul_u32_u24_e32 v15, 9, v14
	v_sub_u32_e32 v15, v17, v15
	v_lshrrev_b32_e32 v16, 6, v14
	v_and_b32_e32 v14, 63, v14
	v_lshlrev_b32_e32 v15, 7, v15
	v_lshl_or_b32 v15, v14, 1, v15
	v_mad_u32_u24 v21, v16, s11, v15
	v_or_b32_e32 v17, 0x200, v0
	v_mul_u32_u24_e32 v14, 0x1c72, v17
	v_lshrrev_b32_e32 v14, 16, v14
	v_mul_u32_u24_e32 v15, 9, v14
	v_sub_u32_e32 v15, v17, v15
	v_lshrrev_b32_e32 v16, 6, v14
	v_and_b32_e32 v14, 63, v14
	v_lshlrev_b32_e32 v15, 7, v15
	v_lshl_or_b32 v15, v14, 1, v15
	v_mad_u32_u24 v22, v16, s11, v15
	v_or_b32_e32 v17, 0x300, v0
	v_mul_u32_u24_e32 v14, 0x1c72, v17
	v_lshrrev_b32_e32 v14, 16, v14
	v_mul_u32_u24_e32 v15, 9, v14
	v_sub_u32_e32 v15, v17, v15
	v_lshrrev_b32_e32 v16, 6, v14
	v_and_b32_e32 v14, 63, v14
	v_lshlrev_b32_e32 v15, 7, v15
	v_lshl_or_b32 v15, v14, 1, v15
	v_mad_u32_u24 v23, v16, s11, v15
	v_or_b32_e32 v17, 0x400, v0
	v_mul_u32_u24_e32 v14, 0x1c72, v17
	v_lshrrev_b32_e32 v14, 16, v14
	v_mul_u32_u24_e32 v15, 9, v14
	v_sub_u32_e32 v15, v17, v15
	v_lshrrev_b32_e32 v16, 6, v14
	v_and_b32_e32 v14, 63, v14
	v_lshlrev_b32_e32 v15, 7, v15
	v_lshl_or_b32 v15, v14, 1, v15
	v_mad_u32_u24 v24, v16, s11, v15
	v_or_b32_e32 v17, 0x500, v0
	v_mul_u32_u24_e32 v14, 0x1c72, v17
	v_lshrrev_b32_e32 v14, 16, v14
	v_mul_u32_u24_e32 v15, 9, v14
	v_sub_u32_e32 v15, v17, v15
	v_lshrrev_b32_e32 v16, 6, v14
	v_and_b32_e32 v14, 63, v14
	v_lshlrev_b32_e32 v15, 7, v15
	v_lshl_or_b32 v15, v14, 1, v15
	v_mad_u32_u24 v25, v16, s11, v15
	v_or_b32_e32 v17, 0x600, v0
	v_mul_u32_u24_e32 v14, 0x1c72, v17
	v_lshrrev_b32_e32 v14, 16, v14
	v_mul_u32_u24_e32 v15, 9, v14
	v_sub_u32_e32 v15, v17, v15
	v_lshrrev_b32_e32 v16, 6, v14
	v_and_b32_e32 v14, 63, v14
	v_lshlrev_b32_e32 v15, 7, v15
	v_lshl_or_b32 v15, v14, 1, v15
	v_mad_u32_u24 v26, v16, s11, v15
	v_or_b32_e32 v17, 0x700, v0
	v_mul_u32_u24_e32 v14, 0x1c72, v17
	v_lshrrev_b32_e32 v14, 16, v14
	v_mul_u32_u24_e32 v15, 9, v14
	v_sub_u32_e32 v15, v17, v15
	v_lshrrev_b32_e32 v16, 6, v14
	v_and_b32_e32 v14, 63, v14
	v_lshlrev_b32_e32 v15, 7, v15
	v_lshl_or_b32 v15, v14, 1, v15
	v_mad_u32_u24 v27, v16, s11, v15
	v_or_b32_e32 v17, 0x800, v0
	v_mul_u32_u24_e32 v14, 0x1c72, v17
	v_lshrrev_b32_e32 v14, 16, v14
	v_mul_u32_u24_e32 v15, 9, v14
	v_sub_u32_e32 v15, v17, v15
	v_lshrrev_b32_e32 v16, 6, v14
	v_and_b32_e32 v14, 63, v14
	v_lshlrev_b32_e32 v15, 7, v15
	v_lshl_or_b32 v15, v14, 1, v15
	v_mad_u32_u24 v28, v16, s11, v15
	s_mov_b32 s5, 0
	s_waitcnt vmcnt(8)
	v_cvt_f16_f32_e32 v1, v1
	s_waitcnt vmcnt(7)
	v_cvt_f16_f32_e32 v6, v6
	s_waitcnt vmcnt(6)
	v_cvt_f16_f32_e32 v7, v7
	s_waitcnt vmcnt(5)
	v_cvt_f16_f32_e32 v8, v8
	s_waitcnt vmcnt(4)
	v_cvt_f16_f32_e32 v10, v10
	s_waitcnt vmcnt(3)
	v_cvt_f16_f32_e32 v11, v11
	s_waitcnt vmcnt(2)
	v_cvt_f16_f32_e32 v12, v12
	s_waitcnt vmcnt(1)
	v_cvt_f16_f32_e32 v13, v13
	ds_write_b16 v20, v1
	ds_write_b16 v21, v6
	ds_write_b16 v22, v7
	ds_write_b16 v23, v8
	ds_write_b16 v24, v10
	ds_write_b16 v25, v11
	ds_write_b16 v26, v12
	ds_write_b16 v27, v13
	s_waitcnt vmcnt(0)
	v_cvt_f16_f32_e32 v2, v5
	s_movk_i32 s4, 0x120
	v_cmp_gt_u32_e32 vcc, s4, v0
	ds_write_b16 v28, v2
	s_waitcnt lgkmcnt(0)
	s_barrier
	s_and_saveexec_b64 s[6:7], vcc
	s_cbranch_execz .LBB0_184
	s_load_dwordx2 s[10:11], s[0:1], 0x50
	s_mul_i32 s4, s3, 0x900
	s_lshl_b64 s[4:5], s[4:5], 1
	v_lshlrev_b32_e32 v2, 4, v0
	v_or_b32_e32 v1, 0xffffff00, v0
	s_waitcnt lgkmcnt(0)
	s_add_u32 s4, s10, s4
	s_addc_u32 s5, s11, s5
	v_lshl_add_u64 v[4:5], s[4:5], 0, v[2:3]
	s_mov_b64 s[4:5], 0
	s_mov_b64 s[10:11], 0x1000

.LBB1_39:
	v_mov_b32_e32 v89, 0
	v_cmp_gt_u32_e32 vcc, s15, v128
	v_mov_b32_e32 v88, v89
	s_and_saveexec_b64 s[8:9], vcc
	s_cbranch_execz .LBB1_43
	s_mul_i32 s13, s15, s69
	s_add_i32 s71, s13, s33
	v_mov_b32_e32 v88, 0
	s_add_i32 s71, s71, s12
	s_mov_b64 s[12:13], 0
	v_mov_b32_e32 v90, v128
	v_mov_b32_e32 v89, v88
.LBB1_41:
	v_add_u32_e32 v92, s71, v90
	v_ashrrev_i32_e32 v93, 31, v92
	v_lshlrev_b64 v[92:93], 8, v[92:93]
	v_lshl_add_u64 v[92:93], v[84:85], 0, v[92:93]
	global_load_dwordx2 v[94:95], v[92:93], off
	s_nop 0
	global_load_dwordx2 v[92:93], v[92:93], off offset:128
	v_add_u32_e32 v90, 16, v90
	v_cmp_le_u32_e32 vcc, s15, v90
	s_or_b64 s[12:13], vcc, s[12:13]
	s_waitcnt vmcnt(0)
	v_pk_add_f32 v[92:93], v[94:95], v[92:93]
	s_nop 0
	v_pk_add_f32 v[88:89], v[88:89], v[92:93]
	s_andn2_b64 exec, exec, s[12:13]
	s_cbranch_execnz .LBB1_41
	s_or_b64 exec, exec, s[12:13]

.LBB1_81:
	s_barrier
	s_setprio 2
	s_mov_b32 m0, s37
	v_add_u32_e32 v0, s48, v211
	global_load_lds_dwordx4 v0, s[10:11]
	v_add_u32_e32 v0, s48, v212
	s_mov_b32 m0, s38
	s_nop 0
	global_load_lds_dwordx4 v0, s[10:11]
	s_setprio 0
	s_setprio 2
	v_mbcnt_lo_u32_b32 v248, -1, 0
	v_mbcnt_hi_u32_b32 v248, -1, v248
	v_mul_u32_u24_e32 v251, 57, v248
	v_lshrrev_b32_e32 v251, 9, v251
	v_mul_u32_u24_e32 v252, 9, v251
	v_sub_u32_e32 v252, v248, v252
	v_mul_u32_u24_e32 v253, 11, v252
	v_lshrrev_b32_e32 v253, 5, v253
	v_mul_u32_u24_e32 v254, 3, v253
	v_sub_u32_e32 v254, v252, v254
	v_add_u32_e32 v253, -1, v253
	v_mul_lo_u32 v253, v253, s50
	v_add3_u32 v253, v253, v254, -1
	v_lshlrev_b32_e32 v253, 9, v253
	v_lshl_add_u32 v253, v251, 7, v253
	v_add_u32_e32 v248, s47, v253
	v_add_u32_e32 v249, 0x10000, v206
	v_add_u32_e32 v250, 0x10000, v213
	v_readlane_b32 s3, v248, 1
	s_mov_b32 m0, s39
	s_nop 1
	v_add_u32_e32 v0, s3, v206
	global_load_lds_dwordx4 v0, s[18:19]
	v_add_u32_e32 v0, s3, v213
	s_mov_b32 m0, s40
	s_nop 0
	global_load_lds_dwordx4 v0, s[18:19]
	s_setprio 0
	s_setprio 2
	s_mov_b32 m0, s41
	v_add_u32_e32 v0, s48, v214
	global_load_lds_dwordx4 v0, s[10:11]
	v_add_u32_e32 v0, s48, v215
	s_mov_b32 m0, s42
	s_nop 0
	global_load_lds_dwordx4 v0, s[10:11]
	s_setprio 0
	s_waitcnt vmcnt(6)
	v_mov_b32_e32 v0, 0
	s_add_i32 s3, s47, 0xfe00
	s_lshl_b32 s6, s50, 23
	v_add_u32_e32 v128, s48, v218
	s_mov_b32 s8, 0
	s_movk_i32 s7, 0x180
	v_mov_b32_e32 v1, v0
	v_mov_b32_e32 v2, v0
	v_mov_b32_e32 v3, v0
	v_mov_b32_e32 v4, v0
	v_mov_b32_e32 v5, v0
	v_mov_b32_e32 v6, v0
	v_mov_b32_e32 v7, v0
	v_mov_b32_e32 v8, v0
	v_mov_b32_e32 v9, v0
	v_mov_b32_e32 v10, v0
	v_mov_b32_e32 v11, v0
	v_mov_b32_e32 v12, v0
	v_mov_b32_e32 v13, v0
	v_mov_b32_e32 v14, v0
	v_mov_b32_e32 v15, v0
	v_mov_b32_e32 v16, v0
	v_mov_b32_e32 v17, v0
	v_mov_b32_e32 v18, v0
	v_mov_b32_e32 v19, v0
	v_mov_b32_e32 v20, v0
	v_mov_b32_e32 v21, v0
	v_mov_b32_e32 v22, v0
	v_mov_b32_e32 v23, v0
	v_mov_b32_e32 v24, v0
	v_mov_b32_e32 v25, v0
	v_mov_b32_e32 v26, v0
	v_mov_b32_e32 v27, v0
	v_mov_b32_e32 v28, v0
	v_mov_b32_e32 v29, v0
	v_mov_b32_e32 v30, v0
	v_mov_b32_e32 v31, v0
	v_mov_b32_e32 v32, v0
	v_mov_b32_e32 v33, v0
	v_mov_b32_e32 v34, v0
	v_mov_b32_e32 v35, v0
	v_mov_b32_e32 v36, v0
	v_mov_b32_e32 v37, v0
	v_mov_b32_e32 v38, v0
	v_mov_b32_e32 v39, v0
	v_mov_b32_e32 v40, v0
	v_mov_b32_e32 v41, v0
	v_mov_b32_e32 v42, v0
	v_mov_b32_e32 v43, v0
	v_mov_b32_e32 v52, v0
	v_mov_b32_e32 v53, v0
	v_mov_b32_e32 v54, v0
	v_mov_b32_e32 v55, v0
	v_mov_b32_e32 v96, v0
	v_mov_b32_e32 v97, v0
	v_mov_b32_e32 v98, v0
	v_mov_b32_e32 v99, v0
	v_mov_b32_e32 v100, v0
	v_mov_b32_e32 v101, v0
	v_mov_b32_e32 v102, v0
	v_mov_b32_e32 v103, v0
	v_mov_b32_e32 v104, v0
	v_mov_b32_e32 v105, v0
	v_mov_b32_e32 v106, v0
	v_mov_b32_e32 v107, v0
	v_mov_b32_e32 v108, v0
	v_mov_b32_e32 v109, v0
	v_mov_b32_e32 v110, v0
	v_mov_b32_e32 v111, v0
	v_mov_b32_e32 v112, v0
	v_mov_b32_e32 v113, v0
	v_mov_b32_e32 v114, v0
	v_mov_b32_e32 v115, v0
	v_mov_b32_e32 v116, v0
	v_mov_b32_e32 v117, v0
	v_mov_b32_e32 v118, v0
	v_mov_b32_e32 v119, v0
	v_mov_b32_e32 v120, v0
	v_mov_b32_e32 v121, v0
	v_mov_b32_e32 v122, v0
	v_mov_b32_e32 v123, v0
	v_mov_b32_e32 v124, v0
	v_mov_b32_e32 v125, v0
	v_mov_b32_e32 v126, v0
	v_mov_b32_e32 v127, v0
	v_mov_b32_e32 v44, v0
	v_mov_b32_e32 v45, v0
	v_mov_b32_e32 v46, v0
	v_mov_b32_e32 v47, v0
	v_mov_b32_e32 v48, v0
	v_mov_b32_e32 v49, v0
	v_mov_b32_e32 v50, v0
	v_mov_b32_e32 v51, v0
	v_mov_b32_e32 v56, v0
	v_mov_b32_e32 v57, v0
	v_mov_b32_e32 v58, v0
	v_mov_b32_e32 v59, v0
	v_mov_b32_e32 v60, v0
	v_mov_b32_e32 v61, v0
	v_mov_b32_e32 v62, v0
	v_mov_b32_e32 v63, v0
	v_mov_b32_e32 v64, v0
	v_mov_b32_e32 v65, v0
	v_mov_b32_e32 v66, v0
	v_mov_b32_e32 v67, v0
	v_mov_b32_e32 v68, v0
	v_mov_b32_e32 v69, v0
	v_mov_b32_e32 v70, v0
	v_mov_b32_e32 v71, v0
	v_mov_b32_e32 v72, v0
	v_mov_b32_e32 v73, v0
	v_mov_b32_e32 v74, v0
	v_mov_b32_e32 v75, v0
	v_mov_b32_e32 v76, v0
	v_mov_b32_e32 v77, v0
	v_mov_b32_e32 v78, v0
	v_mov_b32_e32 v79, v0
	v_mov_b32_e32 v80, v0
	v_mov_b32_e32 v81, v0
	v_mov_b32_e32 v82, v0
	v_mov_b32_e32 v83, v0
	v_mov_b32_e32 v84, v0
	v_mov_b32_e32 v85, v0
	v_mov_b32_e32 v86, v0
	v_mov_b32_e32 v87, v0
	v_mov_b32_e32 v88, v0
	v_mov_b32_e32 v89, v0
	v_mov_b32_e32 v90, v0
	v_mov_b32_e32 v91, v0
	v_mov_b32_e32 v92, v0
	v_mov_b32_e32 v93, v0
	v_mov_b32_e32 v94, v0
	v_mov_b32_e32 v95, v0
	s_barrier
.LBB1_82:
	ds_read_b128 v[130:133], v219 offset:32768
	ds_read_b128 v[134:137], v219 offset:33792
	ds_read_b128 v[138:141], v219 offset:34816
	ds_read_b128 v[142:145], v219 offset:35840
	ds_read_b128 v[146:149], v220
	ds_read_b128 v[150:153], v220 offset:1024
	ds_read_b128 v[154:157], v221
	ds_read_b128 v[158:161], v221 offset:1024
	ds_read_b128 v[162:165], v222
	ds_read_b128 v[166:169], v222 offset:1024
	ds_read_b128 v[170:173], v223
	ds_read_b128 v[174:177], v223 offset:1024
	s_setprio 2
	s_add_i32 s12, s8, 1
	v_readlane_b32 s9, v248, s12
	s_mov_b32 m0, s43
	s_nop 1
	v_add_u32_e32 v129, s9, v249
	global_load_lds_dwordx4 v129, s[18:19]
	v_add_u32_e32 v129, s9, v250
	s_mov_b32 m0, s44
	s_nop 0
	global_load_lds_dwordx4 v129, s[18:19]
	s_setprio 0
	s_waitcnt lgkmcnt(8)
	s_barrier
	s_waitcnt lgkmcnt(0)
	s_setprio 1
	s_waitcnt lgkmcnt(0)
	v_mfma_f32_16x16x32_f16 v[124:127], v[130:133], v[146:149], v[124:127]
	v_mfma_f32_16x16x32_f16 v[120:123], v[138:141], v[146:149], v[120:123]
	v_mfma_f32_16x16x32_f16 v[116:119], v[130:133], v[154:157], v[116:119]
	v_mfma_f32_16x16x32_f16 v[112:115], v[138:141], v[154:157], v[112:115]
	v_mfma_f32_16x16x32_f16 v[108:111], v[130:133], v[162:165], v[108:111]
	v_mfma_f32_16x16x32_f16 v[104:107], v[138:141], v[162:165], v[104:107]
	v_mfma_f32_16x16x32_f16 v[100:103], v[130:133], v[170:173], v[100:103]
	v_mfma_f32_16x16x32_f16 v[96:99], v[138:141], v[170:173], v[96:99]
	v_mfma_f32_16x16x32_f16 v[124:127], v[134:137], v[150:153], v[124:127]
	v_mfma_f32_16x16x32_f16 v[120:123], v[142:145], v[150:153], v[120:123]
	v_mfma_f32_16x16x32_f16 v[116:119], v[134:137], v[158:161], v[116:119]
	v_mfma_f32_16x16x32_f16 v[112:115], v[142:145], v[158:161], v[112:115]
	v_mfma_f32_16x16x32_f16 v[108:111], v[134:137], v[166:169], v[108:111]
	v_mfma_f32_16x16x32_f16 v[104:107], v[142:145], v[166:169], v[104:107]
	v_mfma_f32_16x16x32_f16 v[100:103], v[134:137], v[174:177], v[100:103]
	v_mfma_f32_16x16x32_f16 v[96:99], v[142:145], v[174:177], v[96:99]
	s_setprio 0
	s_barrier
	ds_read_b128 v[178:181], v219 offset:49152
	ds_read_b128 v[182:185], v219 offset:50176
	ds_read_b128 v[186:189], v219 offset:51200
	ds_read_b128 v[190:193], v219 offset:52224
	s_setprio 2
	v_add_u32_e32 v129, s7, v128
	s_mov_b32 m0, s22
	v_add_u32_e32 v194, 0xffffff80, v129
	global_load_lds_dwordx4 v194, s[10:11]
	v_add_u32_e32 v194, 0x47f80, v129
	s_mov_b32 m0, s23
	s_add_i32 s9, s8, 2
	global_load_lds_dwordx4 v194, s[10:11]
	s_setprio 0
	s_barrier
	s_waitcnt lgkmcnt(0)
	s_setprio 1
	s_waitcnt lgkmcnt(0)
	v_mfma_f32_16x16x32_f16 v[52:55], v[178:181], v[146:149], v[52:55]
	v_mfma_f32_16x16x32_f16 v[40:43], v[186:189], v[146:149], v[40:43]
	v_mfma_f32_16x16x32_f16 v[36:39], v[178:181], v[154:157], v[36:39]
	v_mfma_f32_16x16x32_f16 v[32:35], v[186:189], v[154:157], v[32:35]
	v_mfma_f32_16x16x32_f16 v[28:31], v[178:181], v[162:165], v[28:31]
	v_mfma_f32_16x16x32_f16 v[24:27], v[186:189], v[162:165], v[24:27]
	v_mfma_f32_16x16x32_f16 v[20:23], v[178:181], v[170:173], v[20:23]
	v_mfma_f32_16x16x32_f16 v[16:19], v[186:189], v[170:173], v[16:19]
	v_mfma_f32_16x16x32_f16 v[52:55], v[182:185], v[150:153], v[52:55]
	v_mfma_f32_16x16x32_f16 v[40:43], v[190:193], v[150:153], v[40:43]
	v_mfma_f32_16x16x32_f16 v[36:39], v[182:185], v[158:161], v[36:39]
	v_mfma_f32_16x16x32_f16 v[32:35], v[190:193], v[158:161], v[32:35]
	v_mfma_f32_16x16x32_f16 v[28:31], v[182:185], v[166:169], v[28:31]
	v_mfma_f32_16x16x32_f16 v[24:27], v[190:193], v[166:169], v[24:27]
	v_mfma_f32_16x16x32_f16 v[20:23], v[182:185], v[174:177], v[20:23]
	v_mfma_f32_16x16x32_f16 v[16:19], v[190:193], v[174:177], v[16:19]
	s_setprio 0
	s_barrier
	ds_read_b128 v[146:149], v220 offset:16384
	ds_read_b128 v[150:153], v220 offset:17408
	ds_read_b128 v[154:157], v221 offset:16384
	ds_read_b128 v[158:161], v221 offset:17408
	ds_read_b128 v[162:165], v222 offset:16384
	ds_read_b128 v[166:169], v222 offset:17408
	ds_read_b128 v[170:173], v223 offset:16384
	ds_read_b128 v[174:177], v223 offset:17408
	s_setprio 2
	v_readlane_b32 s13, v248, s9
	s_mov_b32 m0, s21
	s_nop 1
	v_add_u32_e32 v194, s13, v206
	global_load_lds_dwordx4 v194, s[18:19]
	v_add_u32_e32 v194, s13, v213
	s_mov_b32 m0, s24
	s_nop 0
	global_load_lds_dwordx4 v194, s[18:19]
	s_setprio 0
	s_barrier
	s_waitcnt lgkmcnt(0)
	s_setprio 1
	s_waitcnt lgkmcnt(0)
	v_mfma_f32_16x16x32_f16 v[12:15], v[130:133], v[146:149], v[12:15]
	v_mfma_f32_16x16x32_f16 v[8:11], v[138:141], v[146:149], v[8:11]
	v_mfma_f32_16x16x32_f16 v[4:7], v[130:133], v[154:157], v[4:7]
	v_mfma_f32_16x16x32_f16 v[0:3], v[138:141], v[154:157], v[0:3]
	v_mfma_f32_16x16x32_f16 v[44:47], v[130:133], v[162:165], v[44:47]
	v_mfma_f32_16x16x32_f16 v[48:51], v[138:141], v[162:165], v[48:51]
	v_mfma_f32_16x16x32_f16 v[56:59], v[130:133], v[170:173], v[56:59]
	v_mfma_f32_16x16x32_f16 v[60:63], v[138:141], v[170:173], v[60:63]
	v_mfma_f32_16x16x32_f16 v[12:15], v[134:137], v[150:153], v[12:15]
	v_mfma_f32_16x16x32_f16 v[8:11], v[142:145], v[150:153], v[8:11]
	v_mfma_f32_16x16x32_f16 v[4:7], v[134:137], v[158:161], v[4:7]
	v_mfma_f32_16x16x32_f16 v[0:3], v[142:145], v[158:161], v[0:3]
	v_mfma_f32_16x16x32_f16 v[44:47], v[134:137], v[166:169], v[44:47]
	v_mfma_f32_16x16x32_f16 v[48:51], v[142:145], v[166:169], v[48:51]
	v_mfma_f32_16x16x32_f16 v[56:59], v[134:137], v[174:177], v[56:59]
	v_mfma_f32_16x16x32_f16 v[60:63], v[142:145], v[174:177], v[60:63]
	s_setprio 0
	s_barrier
	s_setprio 2
	s_mov_b32 m0, s25
	v_add_u32_e32 v130, 0x8ff80, v129
	global_load_lds_dwordx4 v130, s[10:11]
	v_add_u32_e32 v130, 0xd7f80, v129
	s_mov_b32 m0, s26
	s_nop 0
	global_load_lds_dwordx4 v130, s[10:11]
	s_setprio 0
	s_waitcnt vmcnt(6)
	s_barrier
	s_setprio 1
	v_mfma_f32_16x16x32_f16 v[64:67], v[178:181], v[146:149], v[64:67]
	v_mfma_f32_16x16x32_f16 v[68:71], v[186:189], v[146:149], v[68:71]
	v_mfma_f32_16x16x32_f16 v[72:75], v[178:181], v[154:157], v[72:75]
	v_mfma_f32_16x16x32_f16 v[76:79], v[186:189], v[154:157], v[76:79]
	v_mfma_f32_16x16x32_f16 v[80:83], v[178:181], v[162:165], v[80:83]
	v_mfma_f32_16x16x32_f16 v[84:87], v[186:189], v[162:165], v[84:87]
	v_mfma_f32_16x16x32_f16 v[88:91], v[178:181], v[170:173], v[88:91]
	v_mfma_f32_16x16x32_f16 v[92:95], v[186:189], v[170:173], v[92:95]
	v_mfma_f32_16x16x32_f16 v[64:67], v[182:185], v[150:153], v[64:67]
	v_mfma_f32_16x16x32_f16 v[68:71], v[190:193], v[150:153], v[68:71]
	v_mfma_f32_16x16x32_f16 v[72:75], v[182:185], v[158:161], v[72:75]
	v_mfma_f32_16x16x32_f16 v[76:79], v[190:193], v[158:161], v[76:79]
	v_mfma_f32_16x16x32_f16 v[80:83], v[182:185], v[166:169], v[80:83]
	v_mfma_f32_16x16x32_f16 v[84:87], v[190:193], v[166:169], v[84:87]
	v_mfma_f32_16x16x32_f16 v[88:91], v[182:185], v[174:177], v[88:91]
	v_mfma_f32_16x16x32_f16 v[92:95], v[190:193], v[174:177], v[92:95]
	s_setprio 0
	s_barrier
	ds_read_b128 v[130:133], v224
	ds_read_b128 v[134:137], v224 offset:1024
	ds_read_b128 v[138:141], v224 offset:2048
	ds_read_b128 v[142:145], v224 offset:3072
	ds_read_b128 v[146:149], v225
	ds_read_b128 v[150:153], v225 offset:1024
	ds_read_b128 v[154:157], v226
	ds_read_b128 v[158:161], v226 offset:1024
	ds_read_b128 v[162:165], v227
	ds_read_b128 v[166:169], v227 offset:1024
	ds_read_b128 v[170:173], v228
	ds_read_b128 v[174:177], v228 offset:1024
	s_setprio 2
	v_readlane_b32 s12, v248, s9
	s_mov_b32 m0, s27
	s_nop 1
	v_add_u32_e32 v178, s12, v249
	global_load_lds_dwordx4 v178, s[18:19]
	v_add_u32_e32 v178, s12, v250
	s_mov_b32 m0, s28
	s_nop 0
	global_load_lds_dwordx4 v178, s[18:19]
	s_setprio 0
	s_waitcnt lgkmcnt(8)
	s_barrier
	s_waitcnt lgkmcnt(0)
	s_setprio 1
	s_waitcnt lgkmcnt(0)
	v_mfma_f32_16x16x32_f16 v[124:127], v[130:133], v[146:149], v[124:127]
	v_mfma_f32_16x16x32_f16 v[120:123], v[138:141], v[146:149], v[120:123]
	v_mfma_f32_16x16x32_f16 v[116:119], v[130:133], v[154:157], v[116:119]
	v_mfma_f32_16x16x32_f16 v[112:115], v[138:141], v[154:157], v[112:115]
	v_mfma_f32_16x16x32_f16 v[108:111], v[130:133], v[162:165], v[108:111]
	v_mfma_f32_16x16x32_f16 v[104:107], v[138:141], v[162:165], v[104:107]
	v_mfma_f32_16x16x32_f16 v[100:103], v[130:133], v[170:173], v[100:103]
	v_mfma_f32_16x16x32_f16 v[96:99], v[138:141], v[170:173], v[96:99]
	v_mfma_f32_16x16x32_f16 v[124:127], v[134:137], v[150:153], v[124:127]
	v_mfma_f32_16x16x32_f16 v[120:123], v[142:145], v[150:153], v[120:123]
	v_mfma_f32_16x16x32_f16 v[116:119], v[134:137], v[158:161], v[116:119]
	v_mfma_f32_16x16x32_f16 v[112:115], v[142:145], v[158:161], v[112:115]
	v_mfma_f32_16x16x32_f16 v[108:111], v[134:137], v[166:169], v[108:111]
	v_mfma_f32_16x16x32_f16 v[104:107], v[142:145], v[166:169], v[104:107]
	v_mfma_f32_16x16x32_f16 v[100:103], v[134:137], v[174:177], v[100:103]
	v_mfma_f32_16x16x32_f16 v[96:99], v[142:145], v[174:177], v[96:99]
	s_setprio 0
	s_barrier
	ds_read_b128 v[178:181], v229
	ds_read_b128 v[182:185], v229 offset:1024
	ds_read_b128 v[186:189], v229 offset:2048
	ds_read_b128 v[190:193], v229 offset:3072
	s_setprio 2
	s_mov_b32 m0, s37
	v_add_u32_e32 v194, 0x48000, v129
	global_load_lds_dwordx4 v129, s[10:11]
	s_mov_b32 m0, s38
	s_add_i32 s12, s8, 3
	global_load_lds_dwordx4 v194, s[10:11]
	s_setprio 0
	s_barrier
	s_waitcnt lgkmcnt(0)
	s_setprio 1
	s_waitcnt lgkmcnt(0)
	v_mfma_f32_16x16x32_f16 v[52:55], v[178:181], v[146:149], v[52:55]
	v_mfma_f32_16x16x32_f16 v[40:43], v[186:189], v[146:149], v[40:43]
	v_mfma_f32_16x16x32_f16 v[36:39], v[178:181], v[154:157], v[36:39]
	v_mfma_f32_16x16x32_f16 v[32:35], v[186:189], v[154:157], v[32:35]
	v_mfma_f32_16x16x32_f16 v[28:31], v[178:181], v[162:165], v[28:31]
	v_mfma_f32_16x16x32_f16 v[24:27], v[186:189], v[162:165], v[24:27]
	v_mfma_f32_16x16x32_f16 v[20:23], v[178:181], v[170:173], v[20:23]
	v_mfma_f32_16x16x32_f16 v[16:19], v[186:189], v[170:173], v[16:19]
	v_mfma_f32_16x16x32_f16 v[52:55], v[182:185], v[150:153], v[52:55]
	v_mfma_f32_16x16x32_f16 v[40:43], v[190:193], v[150:153], v[40:43]
	v_mfma_f32_16x16x32_f16 v[36:39], v[182:185], v[158:161], v[36:39]
	v_mfma_f32_16x16x32_f16 v[32:35], v[190:193], v[158:161], v[32:35]
	v_mfma_f32_16x16x32_f16 v[28:31], v[182:185], v[166:169], v[28:31]
	v_mfma_f32_16x16x32_f16 v[24:27], v[190:193], v[166:169], v[24:27]
	v_mfma_f32_16x16x32_f16 v[20:23], v[182:185], v[174:177], v[20:23]
	v_mfma_f32_16x16x32_f16 v[16:19], v[190:193], v[174:177], v[16:19]
	s_setprio 0
	s_barrier
	ds_read_b128 v[146:149], v230
	ds_read_b128 v[150:153], v230 offset:1024
	ds_read_b128 v[154:157], v231
	ds_read_b128 v[158:161], v231 offset:1024
	ds_read_b128 v[162:165], v232
	ds_read_b128 v[166:169], v232 offset:1024
	ds_read_b128 v[170:173], v233
	ds_read_b128 v[174:177], v233 offset:1024
	s_setprio 2
	v_readlane_b32 s13, v248, s12
	s_mov_b32 m0, s39
	s_nop 1
	v_add_u32_e32 v194, s13, v206
	global_load_lds_dwordx4 v194, s[18:19]
	v_add_u32_e32 v194, s13, v213
	s_mov_b32 m0, s40
	s_nop 0
	global_load_lds_dwordx4 v194, s[18:19]
	s_setprio 0
	s_barrier
	s_waitcnt lgkmcnt(0)
	s_setprio 1
	s_waitcnt lgkmcnt(0)
	v_mfma_f32_16x16x32_f16 v[12:15], v[130:133], v[146:149], v[12:15]
	v_mfma_f32_16x16x32_f16 v[8:11], v[138:141], v[146:149], v[8:11]
	v_mfma_f32_16x16x32_f16 v[4:7], v[130:133], v[154:157], v[4:7]
	v_mfma_f32_16x16x32_f16 v[0:3], v[138:141], v[154:157], v[0:3]
	v_mfma_f32_16x16x32_f16 v[44:47], v[130:133], v[162:165], v[44:47]
	v_mfma_f32_16x16x32_f16 v[48:51], v[138:141], v[162:165], v[48:51]
	v_mfma_f32_16x16x32_f16 v[56:59], v[130:133], v[170:173], v[56:59]
	v_mfma_f32_16x16x32_f16 v[60:63], v[138:141], v[170:173], v[60:63]
	v_mfma_f32_16x16x32_f16 v[12:15], v[134:137], v[150:153], v[12:15]
	v_mfma_f32_16x16x32_f16 v[8:11], v[142:145], v[150:153], v[8:11]
	v_mfma_f32_16x16x32_f16 v[4:7], v[134:137], v[158:161], v[4:7]
	v_mfma_f32_16x16x32_f16 v[0:3], v[142:145], v[158:161], v[0:3]
	v_mfma_f32_16x16x32_f16 v[44:47], v[134:137], v[166:169], v[44:47]
	v_mfma_f32_16x16x32_f16 v[48:51], v[142:145], v[166:169], v[48:51]
	v_mfma_f32_16x16x32_f16 v[56:59], v[134:137], v[174:177], v[56:59]
	v_mfma_f32_16x16x32_f16 v[60:63], v[142:145], v[174:177], v[60:63]
	s_setprio 0
	s_barrier
	s_setprio 2
	s_mov_b32 m0, s41
	v_add_u32_e32 v130, 0x90000, v129
	global_load_lds_dwordx4 v130, s[10:11]
	v_add_u32_e32 v129, 0xd8000, v129
	s_mov_b32 m0, s42
	s_nop 0
	global_load_lds_dwordx4 v129, s[10:11]
	s_setprio 0
	s_waitcnt vmcnt(6)
	s_barrier
	s_setprio 1
	v_mfma_f32_16x16x32_f16 v[64:67], v[178:181], v[146:149], v[64:67]
	v_mfma_f32_16x16x32_f16 v[68:71], v[186:189], v[146:149], v[68:71]
	v_mfma_f32_16x16x32_f16 v[72:75], v[178:181], v[154:157], v[72:75]
	v_mfma_f32_16x16x32_f16 v[76:79], v[186:189], v[154:157], v[76:79]
	v_mfma_f32_16x16x32_f16 v[80:83], v[178:181], v[162:165], v[80:83]
	v_mfma_f32_16x16x32_f16 v[84:87], v[186:189], v[162:165], v[84:87]
	v_mfma_f32_16x16x32_f16 v[88:91], v[178:181], v[170:173], v[88:91]
	v_mfma_f32_16x16x32_f16 v[92:95], v[186:189], v[170:173], v[92:95]
	v_mfma_f32_16x16x32_f16 v[64:67], v[182:185], v[150:153], v[64:67]
	v_mfma_f32_16x16x32_f16 v[68:71], v[190:193], v[150:153], v[68:71]
	v_mfma_f32_16x16x32_f16 v[72:75], v[182:185], v[158:161], v[72:75]
	v_mfma_f32_16x16x32_f16 v[76:79], v[190:193], v[158:161], v[76:79]
	v_mfma_f32_16x16x32_f16 v[80:83], v[182:185], v[166:169], v[80:83]
	v_mfma_f32_16x16x32_f16 v[84:87], v[190:193], v[166:169], v[84:87]
	v_mfma_f32_16x16x32_f16 v[88:91], v[182:185], v[174:177], v[88:91]
	v_mfma_f32_16x16x32_f16 v[92:95], v[190:193], v[174:177], v[92:95]
	s_setprio 0
	s_addk_i32 s7, 0x100
	s_cmp_lt_u32 s8, 32
	s_mov_b32 s8, s9
	s_barrier
	s_cbranch_scc1 .LBB1_82
	ds_read_b128 v[132:135], v219 offset:32768
	ds_read_b128 v[136:139], v219 offset:33792
	ds_read_b128 v[140:143], v219 offset:34816
	ds_read_b128 v[144:147], v219 offset:35840
	ds_read_b128 v[128:131], v220
	ds_read_b128 v[148:151], v220 offset:1024
	ds_read_b128 v[152:155], v221
	ds_read_b128 v[156:159], v221 offset:1024
	ds_read_b128 v[188:191], v222
	ds_read_b128 v[192:195], v222 offset:1024
	ds_read_b128 v[196:199], v223
	ds_read_b128 v[200:203], v223 offset:1024
	s_setprio 2
	s_lshl_b32 s3, s50, 9
	s_add_i32 s3, s47, s3
	s_add_i32 s3, s3, 0x10380
	s_mov_b32 m0, s43
	v_add_u32_e32 v160, s3, v206
	global_load_lds_dwordx4 v160, s[18:19]
	v_add_u32_e32 v160, s3, v213
	s_mov_b32 m0, s44
	s_nop 0
	global_load_lds_dwordx4 v160, s[18:19]
	s_setprio 0
	s_barrier
	s_waitcnt lgkmcnt(0)
	s_setprio 1
	s_waitcnt lgkmcnt(0)
	v_mfma_f32_16x16x32_f16 v[124:127], v[132:135], v[128:131], v[124:127]
	v_mfma_f32_16x16x32_f16 v[120:123], v[140:143], v[128:131], v[120:123]
	v_mfma_f32_16x16x32_f16 v[116:119], v[132:135], v[152:155], v[116:119]
	v_mfma_f32_16x16x32_f16 v[112:115], v[140:143], v[152:155], v[112:115]
	v_mfma_f32_16x16x32_f16 v[108:111], v[132:135], v[188:191], v[108:111]
	v_mfma_f32_16x16x32_f16 v[104:107], v[140:143], v[188:191], v[104:107]
	v_mfma_f32_16x16x32_f16 v[100:103], v[132:135], v[196:199], v[100:103]
	v_mfma_f32_16x16x32_f16 v[96:99], v[140:143], v[196:199], v[96:99]
	v_mfma_f32_16x16x32_f16 v[160:163], v[136:139], v[148:151], v[124:127]
	v_mfma_f32_16x16x32_f16 v[164:167], v[144:147], v[148:151], v[120:123]
	v_mfma_f32_16x16x32_f16 v[168:171], v[136:139], v[156:159], v[116:119]
	v_mfma_f32_16x16x32_f16 v[172:175], v[144:147], v[156:159], v[112:115]
	v_mfma_f32_16x16x32_f16 v[176:179], v[136:139], v[192:195], v[108:111]
	v_mfma_f32_16x16x32_f16 v[180:183], v[144:147], v[192:195], v[104:107]
	v_mfma_f32_16x16x32_f16 v[100:103], v[136:139], v[200:203], v[100:103]
	v_mfma_f32_16x16x32_f16 v[184:187], v[144:147], v[200:203], v[96:99]
	s_setprio 0
	s_barrier
	ds_read_b128 v[104:107], v219 offset:49152
	ds_read_b128 v[108:111], v219 offset:50176
	ds_read_b128 v[116:119], v219 offset:51200
	ds_read_b128 v[236:239], v219 offset:52224
	s_barrier
	s_waitcnt lgkmcnt(0)
	s_setprio 1
	s_waitcnt lgkmcnt(0)
	v_mfma_f32_16x16x32_f16 v[52:55], v[104:107], v[128:131], v[52:55]
	v_mfma_f32_16x16x32_f16 v[40:43], v[116:119], v[128:131], v[40:43]
	v_mfma_f32_16x16x32_f16 v[36:39], v[104:107], v[152:155], v[36:39]
	v_mfma_f32_16x16x32_f16 v[32:35], v[116:119], v[152:155], v[32:35]
	v_mfma_f32_16x16x32_f16 v[28:31], v[104:107], v[188:191], v[28:31]
	v_mfma_f32_16x16x32_f16 v[24:27], v[116:119], v[188:191], v[24:27]
	v_mfma_f32_16x16x32_f16 v[20:23], v[104:107], v[196:199], v[20:23]
	v_mfma_f32_16x16x32_f16 v[16:19], v[116:119], v[196:199], v[16:19]
	v_mfma_f32_16x16x32_f16 v[52:55], v[108:111], v[148:151], v[52:55]
	v_mfma_f32_16x16x32_f16 v[40:43], v[236:239], v[148:151], v[40:43]
	v_mfma_f32_16x16x32_f16 v[36:39], v[108:111], v[156:159], v[36:39]
	v_mfma_f32_16x16x32_f16 v[32:35], v[236:239], v[156:159], v[32:35]
	v_mfma_f32_16x16x32_f16 v[28:31], v[108:111], v[192:195], v[28:31]
	v_mfma_f32_16x16x32_f16 v[24:27], v[236:239], v[192:195], v[24:27]
	v_mfma_f32_16x16x32_f16 v[96:99], v[108:111], v[200:203], v[20:23]
	v_mfma_f32_16x16x32_f16 v[16:19], v[236:239], v[200:203], v[16:19]
	s_setprio 0
	s_barrier
	ds_read_b128 v[20:23], v220 offset:16384
	ds_read_b128 v[148:151], v220 offset:17408
	ds_read_b128 v[152:155], v221 offset:16384
	ds_read_b128 v[156:159], v221 offset:17408
	ds_read_b128 v[188:191], v222 offset:16384
	ds_read_b128 v[192:195], v222 offset:17408
	ds_read_b128 v[196:199], v223 offset:16384
	ds_read_b128 v[200:203], v223 offset:17408
	s_waitcnt vmcnt(4)
	s_barrier
	s_waitcnt lgkmcnt(0)
	s_setprio 1
	s_waitcnt lgkmcnt(0)
	v_mfma_f32_16x16x32_f16 v[0:3], v[140:143], v[152:155], v[0:3]
	v_mfma_f32_16x16x32_f16 v[124:127], v[144:147], v[156:159], v[0:3]
	v_mfma_f32_16x16x32_f16 v[0:3], v[132:135], v[188:191], v[44:47]
	v_mfma_f32_16x16x32_f16 v[128:131], v[136:139], v[192:195], v[0:3]
	v_mfma_f32_16x16x32_f16 v[0:3], v[140:143], v[188:191], v[48:51]
	v_mfma_f32_16x16x32_f16 v[48:51], v[144:147], v[192:195], v[0:3]
	v_mfma_f32_16x16x32_f16 v[0:3], v[132:135], v[196:199], v[56:59]
	v_mfma_f32_16x16x32_f16 v[12:15], v[132:135], v[20:23], v[12:15]
	v_mfma_f32_16x16x32_f16 v[8:11], v[140:143], v[20:23], v[8:11]
	v_mfma_f32_16x16x32_f16 v[4:7], v[132:135], v[152:155], v[4:7]
	v_mfma_f32_16x16x32_f16 v[56:59], v[136:139], v[200:203], v[0:3]
	v_mfma_f32_16x16x32_f16 v[0:3], v[140:143], v[196:199], v[60:63]
	v_mfma_f32_16x16x32_f16 v[112:115], v[136:139], v[148:151], v[12:15]
	v_mfma_f32_16x16x32_f16 v[8:11], v[144:147], v[148:151], v[8:11]
	v_mfma_f32_16x16x32_f16 v[120:123], v[136:139], v[156:159], v[4:7]
	v_mfma_f32_16x16x32_f16 v[60:63], v[144:147], v[200:203], v[0:3]
	s_setprio 0
	s_setprio 1
	v_mfma_f32_16x16x32_f16 v[0:3], v[104:107], v[20:23], v[64:67]
	v_mfma_f32_16x16x32_f16 v[132:135], v[108:111], v[148:151], v[0:3]
	v_mfma_f32_16x16x32_f16 v[0:3], v[116:119], v[20:23], v[68:71]
	v_mfma_f32_16x16x32_f16 v[136:139], v[236:239], v[148:151], v[0:3]
	v_mfma_f32_16x16x32_f16 v[0:3], v[104:107], v[152:155], v[72:75]
	v_mfma_f32_16x16x32_f16 v[140:143], v[108:111], v[156:159], v[0:3]
	v_mfma_f32_16x16x32_f16 v[0:3], v[116:119], v[152:155], v[76:79]
	v_mfma_f32_16x16x32_f16 v[144:147], v[236:239], v[156:159], v[0:3]
	v_mfma_f32_16x16x32_f16 v[0:3], v[104:107], v[188:191], v[80:83]
	v_mfma_f32_16x16x32_f16 v[80:83], v[108:111], v[192:195], v[0:3]
	v_mfma_f32_16x16x32_f16 v[0:3], v[116:119], v[188:191], v[84:87]
	v_mfma_f32_16x16x32_f16 v[148:151], v[236:239], v[192:195], v[0:3]
	v_mfma_f32_16x16x32_f16 v[0:3], v[104:107], v[196:199], v[88:91]
	v_mfma_f32_16x16x32_f16 v[152:155], v[108:111], v[200:203], v[0:3]
	v_mfma_f32_16x16x32_f16 v[0:3], v[116:119], v[196:199], v[92:95]
	v_mfma_f32_16x16x32_f16 v[156:159], v[236:239], v[200:203], v[0:3]
	s_setprio 0
	s_add_i32 s49, s49, s17
	s_cmpk_lt_i32 s49, 0x1c8
	s_cselect_b64 s[6:7], -1, 0
	s_cmpk_gt_i32 s49, 0x1c7
	s_cselect_b64 s[12:13], -1, 0
	s_and_b64 vcc, exec, s[12:13]
	s_mov_b32 s54, s2
	s_mov_b32 s53, s51
	s_mov_b32 s55, s52
	s_barrier
	s_cbranch_vccnz .LBB1_100
	s_cmpk_lt_i32 s49, 0x148
	s_cbranch_scc1 .LBB1_88
	s_cmpk_lt_u32 s49, 0x1a0
	s_cbranch_scc1 .LBB1_89
	s_cmpk_lt_u32 s49, 0x1b8
	s_cbranch_scc1 .LBB1_90
	s_cmpk_lt_u32 s49, 0x1c0
	s_cselect_b32 s47, s45, 0xfffffe40
	s_cselect_b32 s48, 3, 4
	s_mov_b32 s3, 1
	s_cmp_lt_i32 s48, 1
	s_movk_i32 s53, 0x64
	s_cbranch_scc0 .LBB1_91
	s_branch .LBB1_99

	.amdhsa_kernel _Z9conv_gemmPKDF16_S0_PKfPDF16_PfiiS3_S2_iS2_S2_
		.amdhsa_group_segment_fixed_size 0
		.amdhsa_private_segment_fixed_size 0
		.amdhsa_kernarg_size 344
		.amdhsa_user_sgpr_count 2
		.amdhsa_user_sgpr_dispatch_ptr 0
		.amdhsa_user_sgpr_queue_ptr 0
		.amdhsa_user_sgpr_kernarg_segment_ptr 1
		.amdhsa_user_sgpr_dispatch_id 0
		.amdhsa_user_sgpr_kernarg_preload_length 0
		.amdhsa_user_sgpr_kernarg_preload_offset 0
		.amdhsa_user_sgpr_private_segment_size 0
		.amdhsa_uses_dynamic_stack 0
		.amdhsa_enable_private_segment 0
		.amdhsa_system_sgpr_workgroup_id_x 1
		.amdhsa_system_sgpr_workgroup_id_y 0
		.amdhsa_system_sgpr_workgroup_id_z 0
		.amdhsa_system_sgpr_workgroup_info 0
		.amdhsa_system_vgpr_workitem_id 0
		.amdhsa_next_free_vgpr 256
		.amdhsa_next_free_sgpr 72
		.amdhsa_accum_offset 256
		.amdhsa_reserve_vcc 1
		.amdhsa_float_round_mode_32 0
		.amdhsa_float_round_mode_16_64 0
		.amdhsa_float_denorm_mode_32 3
		.amdhsa_float_denorm_mode_16_64 3
		.amdhsa_dx10_clamp 1
		.amdhsa_ieee_mode 1
		.amdhsa_fp16_overflow 0
		.amdhsa_tg_split 0
		.amdhsa_exception_fp_ieee_invalid_op 0
		.amdhsa_exception_fp_denorm_src 0
		.amdhsa_exception_fp_ieee_div_zero 0
		.amdhsa_exception_fp_ieee_overflow 0
		.amdhsa_exception_fp_ieee_underflow 0
		.amdhsa_exception_fp_ieee_inexact 0
		.amdhsa_exception_int_div_zero 0
	.end_amdhsa_kernel

.LBB2_36:
	v_lshrrev_b32_e32 v2, 4, v0
	v_and_b32_e32 v1, 15, v0
	v_mov_b32_e32 v5, 0
	v_cmp_gt_u32_e32 vcc, s41, v1
	v_lshlrev_b32_e32 v2, 3, v2
	v_mov_b32_e32 v4, v5
	s_and_saveexec_b64 s[42:43], vcc
	s_cbranch_execz .LBB2_40
	s_mul_i32 s49, s41, s44
	s_mul_i32 s50, s35, 0x1c8
	v_mov_b32_e32 v3, 0
	s_waitcnt lgkmcnt(0)
	v_lshl_add_u64 v[6:7], s[8:9], 0, v[2:3]
	s_add_i32 s8, s49, s50
	s_add_i32 s48, s8, s48
	s_mov_b64 s[8:9], 0
	v_mov_b32_e32 v10, v1
	v_mov_b32_e32 v4, v3
	v_mov_b32_e32 v5, v3
.LBB2_38:
	v_add_u32_e32 v12, s48, v10
	v_ashrrev_i32_e32 v13, 31, v12
	v_lshlrev_b64 v[12:13], 8, v[12:13]
	v_lshl_add_u64 v[12:13], v[6:7], 0, v[12:13]
	global_load_dwordx2 v[14:15], v[12:13], off
	global_load_dwordx2 v[16:17], v[12:13], off offset:128
	v_add_u32_e32 v10, 16, v10
	v_cmp_le_u32_e32 vcc, s41, v10
	s_or_b64 s[8:9], vcc, s[8:9]
	s_waitcnt vmcnt(0)
	v_pk_add_f32 v[12:13], v[14:15], v[16:17]
	s_nop 0
	v_pk_add_f32 v[4:5], v[4:5], v[12:13]
	s_andn2_b64 exec, exec, s[8:9]
	s_cbranch_execnz .LBB2_38
	s_or_b64 exec, exec, s[8:9]

amdhsa.kernels:
  - .agpr_count:     0
    .args:
      - .offset:         0
        .size:           40
        .value_kind:     by_value
      - .actual_access:  read_only
        .address_space:  global
        .offset:         40
        .size:           8
        .value_kind:     global_buffer
      - .actual_access:  read_only
        .address_space:  global
        .offset:         48
        .size:           8
        .value_kind:     global_buffer
      - .actual_access:  read_only
        .address_space:  global
        .offset:         56
        .size:           8
        .value_kind:     global_buffer
      - .actual_access:  read_only
        .address_space:  global
        .offset:         64
        .size:           8
        .value_kind:     global_buffer
      - .actual_access:  read_only
        .address_space:  global
        .offset:         72
        .size:           8
        .value_kind:     global_buffer
      - .actual_access:  write_only
        .address_space:  global
        .offset:         80
        .size:           8
        .value_kind:     global_buffer
      - .actual_access:  write_only
        .address_space:  global
        .offset:         88
        .size:           8
        .value_kind:     global_buffer
      - .actual_access:  write_only
        .address_space:  global
        .offset:         96
        .size:           8
        .value_kind:     global_buffer
    .group_segment_fixed_size: 16384
    .kernarg_segment_align: 8
    .kernarg_segment_size: 104
    .language:       OpenCL C
    .language_version:
      - 2
      - 0
    .max_flat_workgroup_size: 256
    .name:           _Z8prep_all8FeatPtrsPKfS1_S1_S1_S1_PDF16_S2_S2_
    .private_segment_fixed_size: 0
    .sgpr_count:     26
    .sgpr_spill_count: 0
    .symbol:         _Z8prep_all8FeatPtrsPKfS1_S1_S1_S1_PDF16_S2_S2_.kd
    .uniform_work_group_size: 1
    .uses_dynamic_stack: false
    .vgpr_count:     38
    .vgpr_spill_count: 0
    .wavefront_size: 64
  - .agpr_count:     0
    .args:
      - .address_space:  global
        .offset:         0
        .size:           8
        .value_kind:     global_buffer
      - .address_space:  global
        .offset:         8
        .size:           8
        .value_kind:     global_buffer
      - .actual_access:  read_only
        .address_space:  global
        .offset:         16
        .size:           8
        .value_kind:     global_buffer
      - .actual_access:  write_only
        .address_space:  global
        .offset:         24
        .size:           8
        .value_kind:     global_buffer
      - .actual_access:  write_only
        .address_space:  global
        .offset:         32
        .size:           8
        .value_kind:     global_buffer
      - .offset:         40
        .size:           4
        .value_kind:     by_value
      - .offset:         44
        .size:           4
        .value_kind:     by_value
      - .address_space:  global
        .offset:         48
        .size:           8
        .value_kind:     global_buffer
      - .actual_access:  read_only
        .address_space:  global
        .offset:         56
        .size:           8
        .value_kind:     global_buffer
      - .offset:         64
        .size:           4
        .value_kind:     by_value
      - .actual_access:  read_only
        .address_space:  global
        .offset:         72
        .size:           8
        .value_kind:     global_buffer
      - .actual_access:  read_only
        .address_space:  global
        .offset:         80
        .size:           8
        .value_kind:     global_buffer
      - .offset:         88
        .size:           4
        .value_kind:     hidden_block_count_x
      - .offset:         92
        .size:           4
        .value_kind:     hidden_block_count_y
      - .offset:         96
        .size:           4
        .value_kind:     hidden_block_count_z
      - .offset:         100
        .size:           2
        .value_kind:     hidden_group_size_x
      - .offset:         102
        .size:           2
        .value_kind:     hidden_group_size_y
      - .offset:         104
        .size:           2
        .value_kind:     hidden_group_size_z
      - .offset:         106
        .size:           2
        .value_kind:     hidden_remainder_x
      - .offset:         108
        .size:           2
        .value_kind:     hidden_remainder_y
      - .offset:         110
        .size:           2
        .value_kind:     hidden_remainder_z
      - .offset:         128
        .size:           8
        .value_kind:     hidden_global_offset_x
      - .offset:         136
        .size:           8
        .value_kind:     hidden_global_offset_y
      - .offset:         144
        .size:           8
        .value_kind:     hidden_global_offset_z
      - .offset:         152
        .size:           2
        .value_kind:     hidden_grid_dims
      - .offset:         208
        .size:           4
        .value_kind:     hidden_dynamic_lds_size
    .group_segment_fixed_size: 0
    .kernarg_segment_align: 8
    .kernarg_segment_size: 344
    .language:       OpenCL C
    .language_version:
      - 2
      - 0
    .max_flat_workgroup_size: 512
    .name:           _Z9conv_gemmPKDF16_S0_PKfPDF16_PfiiS3_S2_iS2_S2_
    .private_segment_fixed_size: 0
    .sgpr_count:     78
    .sgpr_spill_count: 0
    .symbol:         _Z9conv_gemmPKDF16_S0_PKfPDF16_PfiiS3_S2_iS2_S2_.kd
    .uniform_work_group_size: 1
    .uses_dynamic_stack: false
    .vgpr_count:     256
    .vgpr_spill_count: 0
    .wavefront_size: 64
  - .agpr_count:     0
    .args:
      - .actual_access:  read_only
        .address_space:  global
        .offset:         0
        .size:           8
        .value_kind:     global_buffer
      - .actual_access:  read_only
        .address_space:  global
        .offset:         8
        .size:           8
        .value_kind:     global_buffer
      - .actual_access:  read_only
        .address_space:  global
        .offset:         16
        .size:           8
        .value_kind:     global_buffer
      - .actual_access:  read_only
        .address_space:  global
        .offset:         24
        .size:           8
        .value_kind:     global_buffer
      - .actual_access:  read_only
        .address_space:  global
        .offset:         32
        .size:           8
        .value_kind:     global_buffer
      - .actual_access:  read_only
        .address_space:  global
        .offset:         40
        .size:           8
        .value_kind:     global_buffer
      - .actual_access:  read_only
        .address_space:  global
        .offset:         48
        .size:           8
        .value_kind:     global_buffer
      - .actual_access:  read_only
        .address_space:  global
        .offset:         56
        .size:           8
        .value_kind:     global_buffer
      - .actual_access:  read_only
        .address_space:  global
        .offset:         64
        .size:           8
        .value_kind:     global_buffer
      - .actual_access:  read_only
        .address_space:  global
        .offset:         72
        .size:           8
        .value_kind:     global_buffer
      - .actual_access:  read_only
        .address_space:  global
        .offset:         80
        .size:           8
        .value_kind:     global_buffer
      - .actual_access:  write_only
        .address_space:  global
        .offset:         88
        .size:           8
        .value_kind:     global_buffer
    .group_segment_fixed_size: 49152
    .kernarg_segment_align: 8
    .kernarg_segment_size: 96
    .language:       OpenCL C
    .language_version:
      - 2
      - 0
    .max_flat_workgroup_size: 512
    .name:           _Z10head_fusedPKDF16_S0_S0_PKfS2_S2_S2_S2_S2_S2_S2_Pf
    .private_segment_fixed_size: 0
    .sgpr_count:     57
    .sgpr_spill_count: 0
    .symbol:         _Z10head_fusedPKDF16_S0_S0_PKfS2_S2_S2_S2_S2_S2_S2_Pf.kd
    .uniform_work_group_size: 1
    .uses_dynamic_stack: false
    .vgpr_count:     94
    .vgpr_spill_count: 0
    .wavefront_size: 64
